# MoE down-projection epilogue: the 16 LIST/LISTW loads of the 8 row blocks hoisted above the first block (one wait instead of 8 load-store-load chains)
# baseline (speedup 1.0000x reference)
.LBB0_1963:
	v_lshlrev_b32_e32 v4, 2, v208
	v_add_u32_e32 v4, 0, v4
	v_mov_b32_e32 v2, v199
	v_mov_b32_e32 v3, v198
	v_add_u32_e32 v4, 0x20040, v4
	ds_read_b32 v5, v4
	v_add_u32_e32 v4, s68, v2
	v_mul_lo_u32 v6, v208, s87
	v_cmp_lt_i32_e32 vcc, v4, v1
	s_waitcnt lgkmcnt(0)
	v_sub_u32_e32 v2, s34, v5
	v_lshlrev_b32_e32 v5, 8, v2
	v_lshlrev_b32_e32 v2, 3, v3
	v_ashrrev_i32_e32 v3, 31, v2
	v_add_u32_e32 v5, v5, v6
	v_mov_b32_e32 v10, v4
	v_cmp_lt_i32_e32 vcc, v10, v1
	s_and_saveexec_b64 s[10:11], vcc
	s_cbranch_execz .Lm2pf_43699_0
	v_add_u32_e32 v10, v5, v10
	v_ashrrev_i32_e32 v11, 31, v10
	v_lshlrev_b64 v[10:11], 2, v[10:11]
	v_lshl_add_u64 v[12:13], s[26:27], 0, v[10:11]
	v_lshl_add_u64 v[10:11], s[28:29], 0, v[10:11]
	global_load_dword v28, v[12:13], off
	global_load_dword v29, v[10:11], off
.Lm2pf_43699_0:
	s_or_b64 exec, exec, s[10:11]
	v_add_u32_e32 v10, 16, v4
	v_cmp_lt_i32_e32 vcc, v10, v1
	s_and_saveexec_b64 s[10:11], vcc
	s_cbranch_execz .Lm2pf_43699_1
	v_add_u32_e32 v10, v5, v10
	v_ashrrev_i32_e32 v11, 31, v10
	v_lshlrev_b64 v[10:11], 2, v[10:11]
	v_lshl_add_u64 v[12:13], s[26:27], 0, v[10:11]
	v_lshl_add_u64 v[10:11], s[28:29], 0, v[10:11]
	global_load_dword v30, v[12:13], off
	global_load_dword v31, v[10:11], off
.Lm2pf_43699_1:
	s_or_b64 exec, exec, s[10:11]
	v_add_u32_e32 v10, 32, v4
	v_cmp_lt_i32_e32 vcc, v10, v1
	s_and_saveexec_b64 s[10:11], vcc
	s_cbranch_execz .Lm2pf_43699_2
	v_add_u32_e32 v10, v5, v10
	v_ashrrev_i32_e32 v11, 31, v10
	v_lshlrev_b64 v[10:11], 2, v[10:11]
	v_lshl_add_u64 v[12:13], s[26:27], 0, v[10:11]
	v_lshl_add_u64 v[10:11], s[28:29], 0, v[10:11]
	global_load_dword v32, v[12:13], off
	global_load_dword v33, v[10:11], off
.Lm2pf_43699_2:
	s_or_b64 exec, exec, s[10:11]
	v_add_u32_e32 v10, 48, v4
	v_cmp_lt_i32_e32 vcc, v10, v1
	s_and_saveexec_b64 s[10:11], vcc
	s_cbranch_execz .Lm2pf_43699_3
	v_add_u32_e32 v10, v5, v10
	v_ashrrev_i32_e32 v11, 31, v10
	v_lshlrev_b64 v[10:11], 2, v[10:11]
	v_lshl_add_u64 v[12:13], s[26:27], 0, v[10:11]
	v_lshl_add_u64 v[10:11], s[28:29], 0, v[10:11]
	global_load_dword v34, v[12:13], off
	global_load_dword v35, v[10:11], off
.Lm2pf_43699_3:
	s_or_b64 exec, exec, s[10:11]
	v_add_u32_e32 v10, 128, v4
	v_cmp_lt_i32_e32 vcc, v10, v1
	s_and_saveexec_b64 s[10:11], vcc
	s_cbranch_execz .Lm2pf_43699_4
	v_add_u32_e32 v10, v5, v10
	v_ashrrev_i32_e32 v11, 31, v10
	v_lshlrev_b64 v[10:11], 2, v[10:11]
	v_lshl_add_u64 v[12:13], s[26:27], 0, v[10:11]
	v_lshl_add_u64 v[10:11], s[28:29], 0, v[10:11]
	global_load_dword v36, v[12:13], off
	global_load_dword v37, v[10:11], off
.Lm2pf_43699_4:
	s_or_b64 exec, exec, s[10:11]
	v_add_u32_e32 v10, 144, v4
	v_cmp_lt_i32_e32 vcc, v10, v1
	s_and_saveexec_b64 s[10:11], vcc
	s_cbranch_execz .Lm2pf_43699_5
	v_add_u32_e32 v10, v5, v10
	v_ashrrev_i32_e32 v11, 31, v10
	v_lshlrev_b64 v[10:11], 2, v[10:11]
	v_lshl_add_u64 v[12:13], s[26:27], 0, v[10:11]
	v_lshl_add_u64 v[10:11], s[28:29], 0, v[10:11]
	global_load_dword v38, v[12:13], off
	global_load_dword v39, v[10:11], off
.Lm2pf_43699_5:
	s_or_b64 exec, exec, s[10:11]
	v_add_u32_e32 v10, 160, v4
	v_cmp_lt_i32_e32 vcc, v10, v1
	s_and_saveexec_b64 s[10:11], vcc
	s_cbranch_execz .Lm2pf_43699_6
	v_add_u32_e32 v10, v5, v10
	v_ashrrev_i32_e32 v11, 31, v10
	v_lshlrev_b64 v[10:11], 2, v[10:11]
	v_lshl_add_u64 v[12:13], s[26:27], 0, v[10:11]
	v_lshl_add_u64 v[10:11], s[28:29], 0, v[10:11]
	global_load_dword v40, v[12:13], off
	global_load_dword v41, v[10:11], off
.Lm2pf_43699_6:
	s_or_b64 exec, exec, s[10:11]
	v_add_u32_e32 v10, 176, v4
	v_cmp_lt_i32_e32 vcc, v10, v1
	s_and_saveexec_b64 s[10:11], vcc
	s_cbranch_execz .Lm2pf_43699_7
	v_add_u32_e32 v10, v5, v10
	v_ashrrev_i32_e32 v11, 31, v10
	v_lshlrev_b64 v[10:11], 2, v[10:11]
	v_lshl_add_u64 v[12:13], s[26:27], 0, v[10:11]
	v_lshl_add_u64 v[10:11], s[28:29], 0, v[10:11]
	global_load_dword v42, v[12:13], off
	global_load_dword v43, v[10:11], off
.Lm2pf_43699_7:
	s_or_b64 exec, exec, s[10:11]
	s_waitcnt vmcnt(0)
	v_cmp_lt_i32_e32 vcc, v4, v1
	s_and_saveexec_b64 s[10:11], vcc
	s_cbranch_execz .LBB0_1965
	v_add_u32_e32 v6, v5, v4
	v_ashrrev_i32_e32 v7, 31, v6
	v_lshlrev_b64 v[6:7], 2, v[6:7]
	v_lshl_add_u64 v[8:9], s[26:27], 0, v[6:7]
	v_lshl_add_u64 v[6:7], s[28:29], 0, v[6:7]
	v_mov_b32_e32 v8, v28
	s_nop 0
	v_mov_b32_e32 v6, v29
	s_lshl_b32 s38, s58, 8
	s_ashr_i32 s39, s38, 31
	s_lshl_b32 s34, s69, 1
	v_ashrrev_i32_e32 v9, 31, v8
	v_pk_mul_f32 v[14:15], v[188:189], v[6:7] op_sel_hi:[1,0]
	v_lshlrev_b64 v[26:27], 12, v[8:9]
	v_cvt_pk_bf16_f32 v9, v14, v15
	v_lshl_add_u64 v[14:15], s[22:23], 0, v[26:27]
	v_lshl_add_u64 v[14:15], s[38:39], 1, v[14:15]
	v_pk_mul_f32 v[10:11], v[192:193], v[6:7] op_sel_hi:[1,0]
	v_pk_mul_f32 v[12:13], v[190:191], v[6:7] op_sel_hi:[1,0]
	v_pk_mul_f32 v[16:17], v[186:187], v[6:7] op_sel_hi:[1,0]
	v_lshl_add_u64 v[14:15], v[14:15], 0, s[34:35]
	v_pk_mul_f32 v[18:19], v[184:185], v[6:7] op_sel_hi:[1,0]
	v_pk_mul_f32 v[20:21], v[182:183], v[6:7] op_sel_hi:[1,0]
	v_pk_mul_f32 v[22:23], v[180:181], v[6:7] op_sel_hi:[1,0]
	v_pk_mul_f32 v[24:25], v[178:179], v[6:7] op_sel_hi:[1,0]
	v_cvt_pk_bf16_f32 v6, v12, v13
	v_cvt_pk_bf16_f32 v7, v10, v11
	v_cvt_pk_bf16_f32 v8, v16, v17
	v_lshl_add_u64 v[14:15], v[2:3], 1, v[14:15]
	v_cvt_pk_bf16_f32 v10, v20, v21
	v_cvt_pk_bf16_f32 v11, v18, v19
	v_cvt_pk_bf16_f32 v12, v24, v25
	v_cvt_pk_bf16_f32 v13, v22, v23
	global_store_dwordx4 v[14:15], v[6:9], off
	global_store_dwordx4 v[14:15], v[10:13], off offset:256
.LBB0_1965:
	s_or_b64 exec, exec, s[10:11]
	v_add_u32_e32 v6, 16, v4
	v_cmp_lt_i32_e32 vcc, v6, v1
	s_and_saveexec_b64 s[10:11], vcc
	s_cbranch_execz .LBB0_1967
	v_add_u32_e32 v6, v5, v6
	v_ashrrev_i32_e32 v7, 31, v6
	v_lshlrev_b64 v[6:7], 2, v[6:7]
	v_lshl_add_u64 v[8:9], s[26:27], 0, v[6:7]
	v_lshl_add_u64 v[6:7], s[28:29], 0, v[6:7]
	v_mov_b32_e32 v8, v30
	s_nop 0
	v_mov_b32_e32 v6, v31
	s_lshl_b32 s38, s58, 8
	s_ashr_i32 s39, s38, 31
	s_lshl_b32 s34, s69, 1
	v_ashrrev_i32_e32 v9, 31, v8
	v_pk_mul_f32 v[14:15], v[172:173], v[6:7] op_sel_hi:[1,0]
	v_lshlrev_b64 v[26:27], 12, v[8:9]
	v_cvt_pk_bf16_f32 v9, v14, v15
	v_lshl_add_u64 v[14:15], s[22:23], 0, v[26:27]
	v_lshl_add_u64 v[14:15], s[38:39], 1, v[14:15]
	v_pk_mul_f32 v[10:11], v[176:177], v[6:7] op_sel_hi:[1,0]
	v_pk_mul_f32 v[12:13], v[174:175], v[6:7] op_sel_hi:[1,0]
	v_pk_mul_f32 v[16:17], v[170:171], v[6:7] op_sel_hi:[1,0]
	v_lshl_add_u64 v[14:15], v[14:15], 0, s[34:35]
	v_pk_mul_f32 v[18:19], v[168:169], v[6:7] op_sel_hi:[1,0]
	v_pk_mul_f32 v[20:21], v[166:167], v[6:7] op_sel_hi:[1,0]
	v_pk_mul_f32 v[22:23], v[164:165], v[6:7] op_sel_hi:[1,0]
	v_pk_mul_f32 v[24:25], v[162:163], v[6:7] op_sel_hi:[1,0]
	v_cvt_pk_bf16_f32 v6, v12, v13
	v_cvt_pk_bf16_f32 v7, v10, v11
	v_cvt_pk_bf16_f32 v8, v16, v17
	v_lshl_add_u64 v[14:15], v[2:3], 1, v[14:15]
	v_cvt_pk_bf16_f32 v10, v20, v21
	v_cvt_pk_bf16_f32 v11, v18, v19
	v_cvt_pk_bf16_f32 v12, v24, v25
	v_cvt_pk_bf16_f32 v13, v22, v23
	global_store_dwordx4 v[14:15], v[6:9], off
	global_store_dwordx4 v[14:15], v[10:13], off offset:256
.LBB0_1967:
	s_or_b64 exec, exec, s[10:11]
	v_add_u32_e32 v6, 32, v4
	v_cmp_lt_i32_e32 vcc, v6, v1
	s_and_saveexec_b64 s[10:11], vcc
	s_cbranch_execz .LBB0_1969
	v_add_u32_e32 v6, v5, v6
	v_ashrrev_i32_e32 v7, 31, v6
	v_lshlrev_b64 v[6:7], 2, v[6:7]
	v_lshl_add_u64 v[8:9], s[26:27], 0, v[6:7]
	v_lshl_add_u64 v[6:7], s[28:29], 0, v[6:7]
	v_mov_b32_e32 v8, v32
	s_nop 0
	v_mov_b32_e32 v6, v33
	s_lshl_b32 s38, s58, 8
	s_ashr_i32 s39, s38, 31
	s_lshl_b32 s34, s69, 1
	v_ashrrev_i32_e32 v9, 31, v8
	v_pk_mul_f32 v[14:15], v[156:157], v[6:7] op_sel_hi:[1,0]
	v_lshlrev_b64 v[26:27], 12, v[8:9]
	v_cvt_pk_bf16_f32 v9, v14, v15
	v_lshl_add_u64 v[14:15], s[22:23], 0, v[26:27]
	v_lshl_add_u64 v[14:15], s[38:39], 1, v[14:15]
	v_pk_mul_f32 v[10:11], v[160:161], v[6:7] op_sel_hi:[1,0]
	v_pk_mul_f32 v[12:13], v[158:159], v[6:7] op_sel_hi:[1,0]
	v_pk_mul_f32 v[16:17], v[154:155], v[6:7] op_sel_hi:[1,0]
	v_lshl_add_u64 v[14:15], v[14:15], 0, s[34:35]
	v_pk_mul_f32 v[18:19], v[152:153], v[6:7] op_sel_hi:[1,0]
	v_pk_mul_f32 v[20:21], v[150:151], v[6:7] op_sel_hi:[1,0]
	v_pk_mul_f32 v[22:23], v[148:149], v[6:7] op_sel_hi:[1,0]
	v_pk_mul_f32 v[24:25], v[146:147], v[6:7] op_sel_hi:[1,0]
	v_cvt_pk_bf16_f32 v6, v12, v13
	v_cvt_pk_bf16_f32 v7, v10, v11
	v_cvt_pk_bf16_f32 v8, v16, v17
	v_lshl_add_u64 v[14:15], v[2:3], 1, v[14:15]
	v_cvt_pk_bf16_f32 v10, v20, v21
	v_cvt_pk_bf16_f32 v11, v18, v19
	v_cvt_pk_bf16_f32 v12, v24, v25
	v_cvt_pk_bf16_f32 v13, v22, v23
	global_store_dwordx4 v[14:15], v[6:9], off
	global_store_dwordx4 v[14:15], v[10:13], off offset:256
.LBB0_1969:
	s_or_b64 exec, exec, s[10:11]
	v_add_u32_e32 v6, 48, v4
	v_cmp_lt_i32_e32 vcc, v6, v1
	s_and_saveexec_b64 s[10:11], vcc
	s_cbranch_execz .LBB0_1971
	v_add_u32_e32 v6, v5, v6
	v_ashrrev_i32_e32 v7, 31, v6
	v_lshlrev_b64 v[6:7], 2, v[6:7]
	v_lshl_add_u64 v[8:9], s[26:27], 0, v[6:7]
	v_lshl_add_u64 v[6:7], s[28:29], 0, v[6:7]
	v_mov_b32_e32 v8, v34
	s_nop 0
	v_mov_b32_e32 v6, v35
	s_lshl_b32 s38, s58, 8
	s_ashr_i32 s39, s38, 31
	s_lshl_b32 s34, s69, 1
	v_ashrrev_i32_e32 v9, 31, v8
	v_pk_mul_f32 v[14:15], v[140:141], v[6:7] op_sel_hi:[1,0]
	v_lshlrev_b64 v[26:27], 12, v[8:9]
	v_cvt_pk_bf16_f32 v9, v14, v15
	v_lshl_add_u64 v[14:15], s[22:23], 0, v[26:27]
	v_lshl_add_u64 v[14:15], s[38:39], 1, v[14:15]
	v_pk_mul_f32 v[10:11], v[144:145], v[6:7] op_sel_hi:[1,0]
	v_pk_mul_f32 v[12:13], v[142:143], v[6:7] op_sel_hi:[1,0]
	v_pk_mul_f32 v[16:17], v[138:139], v[6:7] op_sel_hi:[1,0]
	v_lshl_add_u64 v[14:15], v[14:15], 0, s[34:35]
	v_pk_mul_f32 v[18:19], v[136:137], v[6:7] op_sel_hi:[1,0]
	v_pk_mul_f32 v[20:21], v[134:135], v[6:7] op_sel_hi:[1,0]
	v_pk_mul_f32 v[22:23], v[132:133], v[6:7] op_sel_hi:[1,0]
	v_pk_mul_f32 v[24:25], v[130:131], v[6:7] op_sel_hi:[1,0]
	v_cvt_pk_bf16_f32 v6, v12, v13
	v_cvt_pk_bf16_f32 v7, v10, v11
	v_cvt_pk_bf16_f32 v8, v16, v17
	v_lshl_add_u64 v[14:15], v[2:3], 1, v[14:15]
	v_cvt_pk_bf16_f32 v10, v20, v21
	v_cvt_pk_bf16_f32 v11, v18, v19
	v_cvt_pk_bf16_f32 v12, v24, v25
	v_cvt_pk_bf16_f32 v13, v22, v23
	global_store_dwordx4 v[14:15], v[6:9], off
	global_store_dwordx4 v[14:15], v[10:13], off offset:256
.LBB0_1971:
	s_or_b64 exec, exec, s[10:11]
	v_add_u32_e32 v6, 0x80, v4
	v_cmp_lt_i32_e32 vcc, v6, v1
	s_and_saveexec_b64 s[10:11], vcc
	s_cbranch_execz .LBB0_1973
	v_add_u32_e32 v6, v5, v6
	v_ashrrev_i32_e32 v7, 31, v6
	v_lshlrev_b64 v[6:7], 2, v[6:7]
	v_lshl_add_u64 v[8:9], s[26:27], 0, v[6:7]
	v_lshl_add_u64 v[6:7], s[28:29], 0, v[6:7]
	v_mov_b32_e32 v8, v36
	s_nop 0
	v_mov_b32_e32 v6, v37
	s_lshl_b32 s38, s58, 8
	s_ashr_i32 s39, s38, 31
	s_lshl_b32 s34, s69, 1
	v_ashrrev_i32_e32 v9, 31, v8
	v_pk_mul_f32 v[14:15], v[124:125], v[6:7] op_sel_hi:[1,0]
	v_lshlrev_b64 v[26:27], 12, v[8:9]
	v_cvt_pk_bf16_f32 v9, v14, v15
	v_lshl_add_u64 v[14:15], s[22:23], 0, v[26:27]
	v_lshl_add_u64 v[14:15], s[38:39], 1, v[14:15]
	v_pk_mul_f32 v[10:11], v[128:129], v[6:7] op_sel_hi:[1,0]
	v_pk_mul_f32 v[12:13], v[126:127], v[6:7] op_sel_hi:[1,0]
	v_pk_mul_f32 v[16:17], v[122:123], v[6:7] op_sel_hi:[1,0]
	v_lshl_add_u64 v[14:15], v[14:15], 0, s[34:35]
	v_pk_mul_f32 v[18:19], v[120:121], v[6:7] op_sel_hi:[1,0]
	v_pk_mul_f32 v[20:21], v[118:119], v[6:7] op_sel_hi:[1,0]
	v_pk_mul_f32 v[22:23], v[116:117], v[6:7] op_sel_hi:[1,0]
	v_pk_mul_f32 v[24:25], v[114:115], v[6:7] op_sel_hi:[1,0]
	v_cvt_pk_bf16_f32 v6, v12, v13
	v_cvt_pk_bf16_f32 v7, v10, v11
	v_cvt_pk_bf16_f32 v8, v16, v17
	v_lshl_add_u64 v[14:15], v[2:3], 1, v[14:15]
	v_cvt_pk_bf16_f32 v10, v20, v21
	v_cvt_pk_bf16_f32 v11, v18, v19
	v_cvt_pk_bf16_f32 v12, v24, v25
	v_cvt_pk_bf16_f32 v13, v22, v23
	global_store_dwordx4 v[14:15], v[6:9], off
	global_store_dwordx4 v[14:15], v[10:13], off offset:256
.LBB0_1973:
	s_or_b64 exec, exec, s[10:11]
	v_add_u32_e32 v6, 0x90, v4
	v_cmp_lt_i32_e32 vcc, v6, v1
	s_and_saveexec_b64 s[10:11], vcc
	s_cbranch_execz .LBB0_1975
	v_add_u32_e32 v6, v5, v6
	v_ashrrev_i32_e32 v7, 31, v6
	v_lshlrev_b64 v[6:7], 2, v[6:7]
	v_lshl_add_u64 v[8:9], s[26:27], 0, v[6:7]
	v_lshl_add_u64 v[6:7], s[28:29], 0, v[6:7]
	v_mov_b32_e32 v8, v38
	s_nop 0
	v_mov_b32_e32 v6, v39
	s_lshl_b32 s38, s58, 8
	s_ashr_i32 s39, s38, 31
	s_lshl_b32 s34, s69, 1
	v_ashrrev_i32_e32 v9, 31, v8
	v_pk_mul_f32 v[14:15], v[108:109], v[6:7] op_sel_hi:[1,0]
	v_lshlrev_b64 v[26:27], 12, v[8:9]
	v_cvt_pk_bf16_f32 v9, v14, v15
	v_lshl_add_u64 v[14:15], s[22:23], 0, v[26:27]
	v_lshl_add_u64 v[14:15], s[38:39], 1, v[14:15]
	v_pk_mul_f32 v[10:11], v[112:113], v[6:7] op_sel_hi:[1,0]
	v_pk_mul_f32 v[12:13], v[110:111], v[6:7] op_sel_hi:[1,0]
	v_pk_mul_f32 v[16:17], v[106:107], v[6:7] op_sel_hi:[1,0]
	v_lshl_add_u64 v[14:15], v[14:15], 0, s[34:35]
	v_pk_mul_f32 v[18:19], v[104:105], v[6:7] op_sel_hi:[1,0]
	v_pk_mul_f32 v[20:21], v[102:103], v[6:7] op_sel_hi:[1,0]
	v_pk_mul_f32 v[22:23], v[100:101], v[6:7] op_sel_hi:[1,0]
	v_pk_mul_f32 v[24:25], v[98:99], v[6:7] op_sel_hi:[1,0]
	v_cvt_pk_bf16_f32 v6, v12, v13
	v_cvt_pk_bf16_f32 v7, v10, v11
	v_cvt_pk_bf16_f32 v8, v16, v17
	v_lshl_add_u64 v[14:15], v[2:3], 1, v[14:15]
	v_cvt_pk_bf16_f32 v10, v20, v21
	v_cvt_pk_bf16_f32 v11, v18, v19
	v_cvt_pk_bf16_f32 v12, v24, v25
	v_cvt_pk_bf16_f32 v13, v22, v23
	global_store_dwordx4 v[14:15], v[6:9], off
	global_store_dwordx4 v[14:15], v[10:13], off offset:256
.LBB0_1975:
	s_or_b64 exec, exec, s[10:11]
	v_add_u32_e32 v6, 0xa0, v4
	v_cmp_lt_i32_e32 vcc, v6, v1
	s_and_saveexec_b64 s[10:11], vcc
	s_cbranch_execz .LBB0_1977
	v_add_u32_e32 v6, v5, v6
	v_ashrrev_i32_e32 v7, 31, v6
	v_lshlrev_b64 v[6:7], 2, v[6:7]
	v_lshl_add_u64 v[8:9], s[26:27], 0, v[6:7]
	v_lshl_add_u64 v[6:7], s[28:29], 0, v[6:7]
	v_mov_b32_e32 v8, v40
	s_nop 0
	v_mov_b32_e32 v6, v41
	s_lshl_b32 s38, s58, 8
	s_ashr_i32 s39, s38, 31
	s_lshl_b32 s34, s69, 1
	v_ashrrev_i32_e32 v9, 31, v8
	v_pk_mul_f32 v[14:15], v[92:93], v[6:7] op_sel_hi:[1,0]
	v_lshlrev_b64 v[26:27], 12, v[8:9]
	v_cvt_pk_bf16_f32 v9, v14, v15
	v_lshl_add_u64 v[14:15], s[22:23], 0, v[26:27]
	v_lshl_add_u64 v[14:15], s[38:39], 1, v[14:15]
	v_pk_mul_f32 v[10:11], v[96:97], v[6:7] op_sel_hi:[1,0]
	v_pk_mul_f32 v[12:13], v[94:95], v[6:7] op_sel_hi:[1,0]
	v_pk_mul_f32 v[16:17], v[90:91], v[6:7] op_sel_hi:[1,0]
	v_lshl_add_u64 v[14:15], v[14:15], 0, s[34:35]
	v_pk_mul_f32 v[18:19], v[88:89], v[6:7] op_sel_hi:[1,0]
	v_pk_mul_f32 v[20:21], v[86:87], v[6:7] op_sel_hi:[1,0]
	v_pk_mul_f32 v[22:23], v[84:85], v[6:7] op_sel_hi:[1,0]
	v_pk_mul_f32 v[24:25], v[82:83], v[6:7] op_sel_hi:[1,0]
	v_cvt_pk_bf16_f32 v6, v12, v13
	v_cvt_pk_bf16_f32 v7, v10, v11
	v_cvt_pk_bf16_f32 v8, v16, v17
	v_lshl_add_u64 v[14:15], v[2:3], 1, v[14:15]
	v_cvt_pk_bf16_f32 v10, v20, v21
	v_cvt_pk_bf16_f32 v11, v18, v19
	v_cvt_pk_bf16_f32 v12, v24, v25
	v_cvt_pk_bf16_f32 v13, v22, v23
	global_store_dwordx4 v[14:15], v[6:9], off
	global_store_dwordx4 v[14:15], v[10:13], off offset:256
.LBB0_1977:
	s_or_b64 exec, exec, s[10:11]
	v_add_u32_e32 v4, 0xb0, v4
	v_cmp_lt_i32_e32 vcc, v4, v1
	s_and_saveexec_b64 s[10:11], vcc
	s_cbranch_execz .LBB0_1979
	v_add_u32_e32 v4, v5, v4
	v_ashrrev_i32_e32 v5, 31, v4
	v_lshlrev_b64 v[4:5], 2, v[4:5]
	v_lshl_add_u64 v[6:7], s[26:27], 0, v[4:5]
	v_lshl_add_u64 v[4:5], s[28:29], 0, v[4:5]
	v_mov_b32_e32 v6, v42
	s_nop 0
	v_mov_b32_e32 v4, v43
	s_lshl_b32 s38, s58, 8
	s_ashr_i32 s39, s38, 31
	s_lshl_b32 s34, s69, 1
	v_ashrrev_i32_e32 v7, 31, v6
	v_pk_mul_f32 v[12:13], v[76:77], v[4:5] op_sel_hi:[1,0]
	v_lshlrev_b64 v[24:25], 12, v[6:7]
	v_cvt_pk_bf16_f32 v7, v12, v13
	v_lshl_add_u64 v[12:13], s[22:23], 0, v[24:25]
	v_lshl_add_u64 v[12:13], s[38:39], 1, v[12:13]
	v_pk_mul_f32 v[8:9], v[80:81], v[4:5] op_sel_hi:[1,0]
	v_pk_mul_f32 v[10:11], v[78:79], v[4:5] op_sel_hi:[1,0]
	v_pk_mul_f32 v[14:15], v[74:75], v[4:5] op_sel_hi:[1,0]
	v_lshl_add_u64 v[12:13], v[12:13], 0, s[34:35]
	v_pk_mul_f32 v[16:17], v[72:73], v[4:5] op_sel_hi:[1,0]
	v_pk_mul_f32 v[18:19], v[70:71], v[4:5] op_sel_hi:[1,0]
	v_pk_mul_f32 v[20:21], v[68:69], v[4:5] op_sel_hi:[1,0]
	v_pk_mul_f32 v[22:23], v[66:67], v[4:5] op_sel_hi:[1,0]
	v_cvt_pk_bf16_f32 v4, v10, v11
	v_cvt_pk_bf16_f32 v5, v8, v9
	v_cvt_pk_bf16_f32 v6, v14, v15
	v_lshl_add_u64 v[2:3], v[2:3], 1, v[12:13]
	v_cvt_pk_bf16_f32 v8, v18, v19
	v_cvt_pk_bf16_f32 v9, v16, v17
	v_cvt_pk_bf16_f32 v10, v22, v23
	v_cvt_pk_bf16_f32 v11, v20, v21
	global_store_dwordx4 v[2:3], v[4:7], off
	global_store_dwordx4 v[2:3], v[8:11], off offset:256
